# stack + P3 scan loads issued together + P1 GEMM rounds 10/2 split with 4-deep p->bf16 loop
# baseline (speedup 1.0000x reference)
.LBB0_137:
	s_cmpk_gt_i32 s0, 0x3fff
	s_cbranch_scc1 .LBB0_140
	s_add_i32 s12, s1, 0xfffff800
	s_ashr_i32 s1, s0, 31
	s_lshl_b64 s[2:3], s[0:1], 9
	s_add_u32 s2, s82, s2
	s_waitcnt vmcnt(0)
	v_lshlrev_b32_e32 v4, 3, v222
	v_mov_b32_e32 v5, 0
	s_addc_u32 s3, s83, s3
	v_lshl_add_u64 v[2:3], s[2:3], 0, v[4:5]
	s_mov_b64 s[2:3], 0x2b00000
	v_lshl_add_u64 v[2:3], v[2:3], 0, s[2:3]
	s_lshl_b64 s[2:3], s[0:1], 10
	s_add_u32 s2, s38, s2
	v_lshlrev_b32_e32 v4, 4, v222
	s_addc_u32 s3, s39, s3
	v_lshl_add_u64 v[4:5], s[2:3], 0, v[4:5]
	s_mov_b64 s[2:3], 0x80000
	s_mov_b64 s[10:11], 0x100000
	s_mov_b32 s12, 4
.LBB0_139:
	global_load_dwordx4 v[6:9], v[4:5], off
	v_lshl_add_u64 v[10:11], v[4:5], 0, s[10:11]
	global_load_dwordx4 v[12:15], v[10:11], off
	v_lshl_add_u64 v[10:11], v[10:11], 0, s[10:11]
	global_load_dwordx4 v[16:19], v[10:11], off
	v_lshl_add_u64 v[10:11], v[10:11], 0, s[10:11]
	global_load_dwordx4 v[20:23], v[10:11], off
	v_lshl_add_u64 v[4:5], v[10:11], 0, s[10:11]
	s_sub_u32 s12, s12, 1
	s_waitcnt vmcnt(3)
	v_cvt_pk_bf16_f32 v6, v6, v7
	v_cvt_pk_bf16_f32 v7, v8, v9
	global_store_dwordx2 v[2:3], v[6:7], off
	v_lshl_add_u64 v[2:3], v[2:3], 0, s[2:3]
	s_waitcnt vmcnt(3)
	v_cvt_pk_bf16_f32 v12, v12, v13
	v_cvt_pk_bf16_f32 v13, v14, v15
	global_store_dwordx2 v[2:3], v[12:13], off
	v_lshl_add_u64 v[2:3], v[2:3], 0, s[2:3]
	s_waitcnt vmcnt(3)
	v_cvt_pk_bf16_f32 v16, v16, v17
	v_cvt_pk_bf16_f32 v17, v18, v19
	global_store_dwordx2 v[2:3], v[16:17], off
	v_lshl_add_u64 v[2:3], v[2:3], 0, s[2:3]
	s_waitcnt vmcnt(3)
	v_cvt_pk_bf16_f32 v20, v20, v21
	v_cvt_pk_bf16_f32 v21, v22, v23
	global_store_dwordx2 v[2:3], v[20:21], off
	v_lshl_add_u64 v[2:3], v[2:3], 0, s[2:3]
	s_cmp_lg_u32 s12, 0
	s_cbranch_scc1 .LBB0_139

.LBB0_144:
	s_andn2_b64 vcc, exec, s[8:9]
	s_cbranch_vccnz .LBB0_146
	s_add_i32 s2, s87, 0xffffff80
	s_and_b64 s[0:1], s[6:7], exec
	s_cselect_b32 s26, s2, s87
	s_cselect_b32 s24, 10, 0
	s_cselect_b32 s25, 2.0, 10
	s_movk_i32 s27, 0x80
	s_branch .LBB0_147

.LBB0_337:
	s_and_b32 s5, s6, 0x3800
	s_and_b32 s4, s8, -16
	v_or_b32_e32 v1, s5, v194
	v_lshlrev_b32_e32 v2, 2, v1
	s_waitcnt vmcnt(0)
	v_lshl_add_u64 v[8:9], s[0:1], 0, v[2:3]
	v_lshlrev_b32_e32 v2, 1, v1
	v_lshl_add_u64 v[6:7], s[2:3], 0, v[2:3]
	s_mov_b32 s13, 0
	s_mov_b32 s15, 0
	s_mov_b32 s17, 0
	s_or_b32 s12, s4, 0
	s_lshl_b64 s[14:15], s[12:13], 16
	s_lshl_b32 s16, s12, 9
	v_lshl_add_u64 v[10:11], v[8:9], 0, s[14:15]
	v_lshl_add_u64 v[12:13], v[4:5], 0, s[16:17]
	global_load_dwordx4 v[40:43], v[10:11], off
	global_load_dwordx4 v[44:47], v[12:13], off
	s_or_b32 s12, s4, 1
	s_lshl_b64 s[14:15], s[12:13], 16
	s_lshl_b32 s16, s12, 9
	v_lshl_add_u64 v[10:11], v[8:9], 0, s[14:15]
	v_lshl_add_u64 v[12:13], v[4:5], 0, s[16:17]
	global_load_dwordx4 v[48:51], v[10:11], off
	global_load_dwordx4 v[52:55], v[12:13], off
	s_or_b32 s12, s4, 2
	s_lshl_b64 s[14:15], s[12:13], 16
	s_lshl_b32 s16, s12, 9
	v_lshl_add_u64 v[10:11], v[8:9], 0, s[14:15]
	v_lshl_add_u64 v[12:13], v[4:5], 0, s[16:17]
	global_load_dwordx4 v[56:59], v[10:11], off
	global_load_dwordx4 v[60:63], v[12:13], off
	s_or_b32 s12, s4, 3
	s_lshl_b64 s[14:15], s[12:13], 16
	s_lshl_b32 s16, s12, 9
	v_lshl_add_u64 v[10:11], v[8:9], 0, s[14:15]
	v_lshl_add_u64 v[12:13], v[4:5], 0, s[16:17]
	global_load_dwordx4 v[64:67], v[10:11], off
	global_load_dwordx4 v[68:71], v[12:13], off
	s_or_b32 s12, s4, 4
	s_lshl_b64 s[14:15], s[12:13], 16
	s_lshl_b32 s16, s12, 9
	v_lshl_add_u64 v[10:11], v[8:9], 0, s[14:15]
	v_lshl_add_u64 v[12:13], v[4:5], 0, s[16:17]
	global_load_dwordx4 v[72:75], v[10:11], off
	global_load_dwordx4 v[76:79], v[12:13], off
	s_or_b32 s12, s4, 5
	s_lshl_b64 s[14:15], s[12:13], 16
	s_lshl_b32 s16, s12, 9
	v_lshl_add_u64 v[10:11], v[8:9], 0, s[14:15]
	v_lshl_add_u64 v[12:13], v[4:5], 0, s[16:17]
	global_load_dwordx4 v[80:83], v[10:11], off
	global_load_dwordx4 v[84:87], v[12:13], off
	s_or_b32 s12, s4, 6
	s_lshl_b64 s[14:15], s[12:13], 16
	s_lshl_b32 s16, s12, 9
	v_lshl_add_u64 v[10:11], v[8:9], 0, s[14:15]
	v_lshl_add_u64 v[12:13], v[4:5], 0, s[16:17]
	global_load_dwordx4 v[88:91], v[10:11], off
	global_load_dwordx4 v[92:95], v[12:13], off
	s_or_b32 s12, s4, 7
	s_lshl_b64 s[14:15], s[12:13], 16
	s_lshl_b32 s16, s12, 9
	v_lshl_add_u64 v[10:11], v[8:9], 0, s[14:15]
	v_lshl_add_u64 v[12:13], v[4:5], 0, s[16:17]
	global_load_dwordx4 v[96:99], v[10:11], off
	global_load_dwordx4 v[100:103], v[12:13], off
	s_or_b32 s12, s4, 8
	s_lshl_b64 s[14:15], s[12:13], 16
	s_lshl_b32 s16, s12, 9
	v_lshl_add_u64 v[10:11], v[8:9], 0, s[14:15]
	v_lshl_add_u64 v[12:13], v[4:5], 0, s[16:17]
	global_load_dwordx4 v[104:107], v[10:11], off
	global_load_dwordx4 v[108:111], v[12:13], off
	s_or_b32 s12, s4, 9
	s_lshl_b64 s[14:15], s[12:13], 16
	s_lshl_b32 s16, s12, 9
	v_lshl_add_u64 v[10:11], v[8:9], 0, s[14:15]
	v_lshl_add_u64 v[12:13], v[4:5], 0, s[16:17]
	global_load_dwordx4 v[112:115], v[10:11], off
	global_load_dwordx4 v[116:119], v[12:13], off
	s_or_b32 s12, s4, 10
	s_lshl_b64 s[14:15], s[12:13], 16
	s_lshl_b32 s16, s12, 9
	v_lshl_add_u64 v[10:11], v[8:9], 0, s[14:15]
	v_lshl_add_u64 v[12:13], v[4:5], 0, s[16:17]
	global_load_dwordx4 v[120:123], v[10:11], off
	global_load_dwordx4 v[124:127], v[12:13], off
	s_or_b32 s12, s4, 11
	s_lshl_b64 s[14:15], s[12:13], 16
	s_lshl_b32 s16, s12, 9
	v_lshl_add_u64 v[10:11], v[8:9], 0, s[14:15]
	v_lshl_add_u64 v[12:13], v[4:5], 0, s[16:17]
	global_load_dwordx4 v[128:131], v[10:11], off
	global_load_dwordx4 v[132:135], v[12:13], off
	s_or_b32 s12, s4, 12
	s_lshl_b64 s[14:15], s[12:13], 16
	s_lshl_b32 s16, s12, 9
	v_lshl_add_u64 v[10:11], v[8:9], 0, s[14:15]
	v_lshl_add_u64 v[12:13], v[4:5], 0, s[16:17]
	global_load_dwordx4 v[136:139], v[10:11], off
	global_load_dwordx4 v[140:143], v[12:13], off
	s_or_b32 s12, s4, 13
	s_lshl_b64 s[14:15], s[12:13], 16
	s_lshl_b32 s16, s12, 9
	v_lshl_add_u64 v[10:11], v[8:9], 0, s[14:15]
	v_lshl_add_u64 v[12:13], v[4:5], 0, s[16:17]
	global_load_dwordx4 v[144:147], v[10:11], off
	global_load_dwordx4 v[148:151], v[12:13], off
	s_or_b32 s12, s4, 14
	s_lshl_b64 s[14:15], s[12:13], 16
	s_lshl_b32 s16, s12, 9
	v_lshl_add_u64 v[10:11], v[8:9], 0, s[14:15]
	v_lshl_add_u64 v[12:13], v[4:5], 0, s[16:17]
	global_load_dwordx4 v[152:155], v[10:11], off
	global_load_dwordx4 v[156:159], v[12:13], off
	s_add_i32 s10, s10, s84
	s_add_i32 s6, s6, s7
	s_add_i32 s8, s8, s9
	s_waitcnt vmcnt(28)
	v_pk_fma_f32 v[24:25], v[46:47], 0, v[42:43] op_sel_hi:[1,0,1]
	v_pk_fma_f32 v[26:27], v[44:45], 0, v[40:41] op_sel_hi:[1,0,1]
	s_or_b32 s12, s4, 1
	s_lshl_b64 s[14:15], s[12:13], 15
	v_cvt_pk_bf16_f32 v15, v24, v25
	v_cvt_pk_bf16_f32 v14, v26, v27
	v_lshl_add_u64 v[16:17], v[6:7], 0, s[14:15]
	global_store_dwordx2 v[16:17], v[14:15], off
	s_waitcnt vmcnt(27)
	v_pk_fma_f32 v[24:25], v[24:25], v[54:55], v[50:51]
	v_pk_fma_f32 v[26:27], v[26:27], v[52:53], v[48:49]
	s_or_b32 s12, s4, 2
	s_lshl_b64 s[14:15], s[12:13], 15
	v_cvt_pk_bf16_f32 v15, v24, v25
	v_cvt_pk_bf16_f32 v14, v26, v27
	v_lshl_add_u64 v[16:17], v[6:7], 0, s[14:15]
	global_store_dwordx2 v[16:17], v[14:15], off
	s_waitcnt vmcnt(26)
	v_pk_fma_f32 v[24:25], v[24:25], v[62:63], v[58:59]
	v_pk_fma_f32 v[26:27], v[26:27], v[60:61], v[56:57]
	s_or_b32 s12, s4, 3
	s_lshl_b64 s[14:15], s[12:13], 15
	v_cvt_pk_bf16_f32 v15, v24, v25
	v_cvt_pk_bf16_f32 v14, v26, v27
	v_lshl_add_u64 v[16:17], v[6:7], 0, s[14:15]
	global_store_dwordx2 v[16:17], v[14:15], off
	s_waitcnt vmcnt(25)
	v_pk_fma_f32 v[24:25], v[24:25], v[70:71], v[66:67]
	v_pk_fma_f32 v[26:27], v[26:27], v[68:69], v[64:65]
	s_or_b32 s12, s4, 4
	s_lshl_b64 s[14:15], s[12:13], 15
	v_cvt_pk_bf16_f32 v15, v24, v25
	v_cvt_pk_bf16_f32 v14, v26, v27
	v_lshl_add_u64 v[16:17], v[6:7], 0, s[14:15]
	global_store_dwordx2 v[16:17], v[14:15], off
	s_waitcnt vmcnt(24)
	v_pk_fma_f32 v[24:25], v[24:25], v[78:79], v[74:75]
	v_pk_fma_f32 v[26:27], v[26:27], v[76:77], v[72:73]
	s_or_b32 s12, s4, 5
	s_lshl_b64 s[14:15], s[12:13], 15
	v_cvt_pk_bf16_f32 v15, v24, v25
	v_cvt_pk_bf16_f32 v14, v26, v27
	v_lshl_add_u64 v[16:17], v[6:7], 0, s[14:15]
	global_store_dwordx2 v[16:17], v[14:15], off
	s_waitcnt vmcnt(23)
	v_pk_fma_f32 v[24:25], v[24:25], v[86:87], v[82:83]
	v_pk_fma_f32 v[26:27], v[26:27], v[84:85], v[80:81]
	s_or_b32 s12, s4, 6
	s_lshl_b64 s[14:15], s[12:13], 15
	v_cvt_pk_bf16_f32 v15, v24, v25
	v_cvt_pk_bf16_f32 v14, v26, v27
	v_lshl_add_u64 v[16:17], v[6:7], 0, s[14:15]
	global_store_dwordx2 v[16:17], v[14:15], off
	s_waitcnt vmcnt(22)
	v_pk_fma_f32 v[24:25], v[24:25], v[94:95], v[90:91]
	v_pk_fma_f32 v[26:27], v[26:27], v[92:93], v[88:89]
	s_or_b32 s12, s4, 7
	s_lshl_b64 s[14:15], s[12:13], 15
	v_cvt_pk_bf16_f32 v15, v24, v25
	v_cvt_pk_bf16_f32 v14, v26, v27
	v_lshl_add_u64 v[16:17], v[6:7], 0, s[14:15]
	global_store_dwordx2 v[16:17], v[14:15], off
	s_waitcnt vmcnt(21)
	v_pk_fma_f32 v[24:25], v[24:25], v[102:103], v[98:99]
	v_pk_fma_f32 v[26:27], v[26:27], v[100:101], v[96:97]
	s_or_b32 s12, s4, 8
	s_lshl_b64 s[14:15], s[12:13], 15
	v_cvt_pk_bf16_f32 v15, v24, v25
	v_cvt_pk_bf16_f32 v14, v26, v27
	v_lshl_add_u64 v[16:17], v[6:7], 0, s[14:15]
	global_store_dwordx2 v[16:17], v[14:15], off
	s_waitcnt vmcnt(20)
	v_pk_fma_f32 v[24:25], v[24:25], v[110:111], v[106:107]
	v_pk_fma_f32 v[26:27], v[26:27], v[108:109], v[104:105]
	s_or_b32 s12, s4, 9
	s_lshl_b64 s[14:15], s[12:13], 15
	v_cvt_pk_bf16_f32 v15, v24, v25
	v_cvt_pk_bf16_f32 v14, v26, v27
	v_lshl_add_u64 v[16:17], v[6:7], 0, s[14:15]
	global_store_dwordx2 v[16:17], v[14:15], off
	s_waitcnt vmcnt(19)
	v_pk_fma_f32 v[24:25], v[24:25], v[118:119], v[114:115]
	v_pk_fma_f32 v[26:27], v[26:27], v[116:117], v[112:113]
	s_or_b32 s12, s4, 10
	s_lshl_b64 s[14:15], s[12:13], 15
	v_cvt_pk_bf16_f32 v15, v24, v25
	v_cvt_pk_bf16_f32 v14, v26, v27
	v_lshl_add_u64 v[16:17], v[6:7], 0, s[14:15]
	global_store_dwordx2 v[16:17], v[14:15], off
	s_waitcnt vmcnt(18)
	v_pk_fma_f32 v[24:25], v[24:25], v[126:127], v[122:123]
	v_pk_fma_f32 v[26:27], v[26:27], v[124:125], v[120:121]
	s_or_b32 s12, s4, 11
	s_lshl_b64 s[14:15], s[12:13], 15
	v_cvt_pk_bf16_f32 v15, v24, v25
	v_cvt_pk_bf16_f32 v14, v26, v27
	v_lshl_add_u64 v[16:17], v[6:7], 0, s[14:15]
	global_store_dwordx2 v[16:17], v[14:15], off
	s_waitcnt vmcnt(17)
	v_pk_fma_f32 v[24:25], v[24:25], v[134:135], v[130:131]
	v_pk_fma_f32 v[26:27], v[26:27], v[132:133], v[128:129]
	s_or_b32 s12, s4, 12
	s_lshl_b64 s[14:15], s[12:13], 15
	v_cvt_pk_bf16_f32 v15, v24, v25
	v_cvt_pk_bf16_f32 v14, v26, v27
	v_lshl_add_u64 v[16:17], v[6:7], 0, s[14:15]
	global_store_dwordx2 v[16:17], v[14:15], off
	s_waitcnt vmcnt(16)
	v_pk_fma_f32 v[24:25], v[24:25], v[142:143], v[138:139]
	v_pk_fma_f32 v[26:27], v[26:27], v[140:141], v[136:137]
	s_or_b32 s12, s4, 13
	s_lshl_b64 s[14:15], s[12:13], 15
	v_cvt_pk_bf16_f32 v15, v24, v25
	v_cvt_pk_bf16_f32 v14, v26, v27
	v_lshl_add_u64 v[16:17], v[6:7], 0, s[14:15]
	global_store_dwordx2 v[16:17], v[14:15], off
	s_waitcnt vmcnt(15)
	v_pk_fma_f32 v[24:25], v[24:25], v[150:151], v[146:147]
	v_pk_fma_f32 v[26:27], v[26:27], v[148:149], v[144:145]
	s_or_b32 s12, s4, 14
	s_lshl_b64 s[14:15], s[12:13], 15
	v_cvt_pk_bf16_f32 v15, v24, v25
	v_cvt_pk_bf16_f32 v14, v26, v27
	v_lshl_add_u64 v[16:17], v[6:7], 0, s[14:15]
	global_store_dwordx2 v[16:17], v[14:15], off
	s_waitcnt vmcnt(14)
	v_pk_fma_f32 v[24:25], v[24:25], v[158:159], v[154:155]
	v_pk_fma_f32 v[26:27], v[26:27], v[156:157], v[152:153]
	s_or_b32 s12, s4, 15
	s_lshl_b64 s[14:15], s[12:13], 15
	v_cvt_pk_bf16_f32 v15, v24, v25
	v_cvt_pk_bf16_f32 v14, v26, v27
	v_lshl_add_u64 v[16:17], v[6:7], 0, s[14:15]
	global_store_dwordx2 v[16:17], v[14:15], off
	s_cmpk_gt_i32 s10, 0xff
	s_cbranch_scc0 .LBB0_337
